# rmsnorm+modulate pass: first dependent op moved behind the whole 16-load burst (one memory round trip per row pair instead of two)
# speedup vs baseline: 1.0015x; 1.0015x over previous
; template <int OUT, bool SRCBF>
; DI void nm_rowpair(LAS unsigned char* lds, const void* src0v, const void* src1v, bf16_t* b0, bf16_t* b1, unsigned char* q0, unsigned char* q1, int lane, float* sc0 = nullptr) {
;     ...
; #pragma unroll
;     for (int j = 0; j < 4; ++j) { const int c = 512 * j + 8 * lane; xa[2 * j] = *(const f32x4*)(src0 + c); xa[2 * j + 1] = *(const f32x4*)(src0 + c + 4); xb[2 * j] = *(const f32x4*)(src1 + c); xb[2 * j + 1] = *(const f32x4*)(src1 + c + 4); } }
; #pragma unroll
;     for (int j = 0; j < 8; ++j) { sa += (xa[j][0] * xa[j][0] + xa[j][1] * xa[j][1]) + (xa[j][2] * xa[j][2] + xa[j][3] * xa[j][3]); sb += (xb[j][0] * xb[j][0] + xb[j][1] * xb[j][1]) + (xb[j][2] * xb[j][2] + xb[j][3] * xb[j][3]); }
;     const float ra = 1.0f / sqrtf(wave_sum(sa) * (1.0f / D) + EPS), rb = 1.0f / sqrtf(wave_sum(sb) * (1.0f / D) + EPS);
.LBB0_206:
	v_lshl_add_u64 v[64:65], v[136:137], 0, s[58:59]
	v_lshl_add_u64 v[66:67], v[64:65], 0, s[44:45]
	global_load_dwordx4 v[120:123], v[64:65], off
	global_load_dwordx4 v[112:115], v[64:65], off offset:16
	global_load_dwordx4 v[108:111], v[64:65], off offset:2048
	global_load_dwordx4 v[104:107], v[64:65], off offset:2064
	global_load_dwordx4 v[116:119], v[66:67], off offset:16
	v_lshl_add_u64 v[66:67], v[64:65], 0, s[50:51]
	global_load_dwordx4 v[96:99], v[66:67], off offset:16
	v_add_co_u32_e32 v66, vcc, s35, v64
	v_lshl_add_u64 v[70:71], v[64:65], 0, s[38:39]
	s_nop 0
	v_addc_co_u32_e32 v67, vcc, 0, v65, vcc
	global_load_dwordx4 v[100:103], v[66:67], off offset:2048
	v_add_co_u32_e32 v66, vcc, s67, v64
	v_lshl_add_u64 v[72:73], v[64:65], 0, s[42:43]
	s_nop 0
	v_addc_co_u32_e32 v67, vcc, 0, v65, vcc
	global_load_dwordx4 v[124:127], v[66:67], off offset:-4096
	v_add_co_u32_e32 v68, vcc, s66, v64
	s_nop 1
	v_addc_co_u32_e32 v69, vcc, 0, v65, vcc
	global_load_dwordx4 v[92:95], v[68:69], off
	global_load_dwordx4 v[84:87], v[66:67], off
	global_load_dwordx4 v[88:91], v[70:71], off offset:16
	v_lshl_add_u64 v[70:71], v[64:65], 0, s[52:53]
	global_load_dwordx4 v[80:83], v[70:71], off offset:16
	global_load_dwordx4 v[76:79], v[68:69], off offset:2048
	v_lshl_add_u64 v[64:65], v[64:65], 0, s[54:55]
	global_load_dwordx4 v[68:71], v[66:67], off offset:2048
	s_nop 0
	global_load_dwordx4 v[72:75], v[72:73], off offset:16
	s_nop 0
	global_load_dwordx4 v[64:67], v[64:65], off offset:16
	s_waitcnt vmcnt(15)
	v_mul_f32_e32 v138, v121, v121
	v_mul_f32_e32 v139, v123, v123
	s_waitcnt vmcnt(14)
	v_mul_f32_e32 v140, v113, v113
	v_mul_f32_e32 v141, v115, v115
	s_waitcnt vmcnt(13)
	v_mul_f32_e32 v142, v109, v109
	v_mul_f32_e32 v143, v111, v111
	s_waitcnt vmcnt(12)
	v_mul_f32_e32 v144, v105, v105
	v_mul_f32_e32 v145, v107, v107
	v_fmac_f32_e32 v138, v120, v120
	v_fmac_f32_e32 v139, v122, v122
	v_fmac_f32_e32 v140, v112, v112
	v_fmac_f32_e32 v141, v114, v114
	v_fmac_f32_e32 v142, v108, v108
	v_fmac_f32_e32 v143, v110, v110
	v_fmac_f32_e32 v144, v104, v104
	v_fmac_f32_e32 v145, v106, v106
	v_add_f32_e32 v138, v138, v139
	v_add_f32_e32 v139, v140, v141
	v_add_f32_e32 v140, v142, v143
	s_waitcnt vmcnt(9)
	v_mul_f32_e32 v141, v101, v101
	v_mul_f32_e32 v142, v103, v103
	v_mul_f32_e32 v154, v117, v117
	v_mul_f32_e32 v155, v119, v119
	v_add_f32_e32 v143, v144, v145
	s_waitcnt vmcnt(8)
	v_mul_f32_e32 v144, v125, v125
	v_mul_f32_e32 v145, v127, v127
	v_add_f32_e32 v138, v138, v139
	v_fmac_f32_e32 v141, v100, v100
	v_fmac_f32_e32 v142, v102, v102
	v_fmac_f32_e32 v154, v116, v116
	v_fmac_f32_e32 v155, v118, v118
	v_fmac_f32_e32 v144, v124, v124
	v_fmac_f32_e32 v145, v126, v126
	v_add_f32_e32 v138, v138, v140
	v_add_f32_e32 v140, v141, v142
	v_add_f32_e32 v139, v154, v155
	v_add_f32_e32 v144, v144, v145
	v_mul_f32_e32 v156, v97, v97
	v_mul_f32_e32 v157, v99, v99
	v_add_f32_e32 v138, v138, v143
	v_add_f32_e32 v139, v144, v139
	v_fmac_f32_e32 v156, v96, v96
	v_fmac_f32_e32 v157, v98, v98
	v_add_f32_e32 v139, v139, v140
	v_add_f32_e32 v154, v156, v157
	v_add_f32_e32 v139, v139, v154
	s_waitcnt vmcnt(7)
	v_mul_f32_e32 v141, v93, v93
	v_mul_f32_e32 v142, v95, v95
	v_fmac_f32_e32 v141, v92, v92
	v_fmac_f32_e32 v142, v94, v94
	v_add_f32_e32 v141, v141, v142
	v_add_f32_e32 v138, v138, v141
	s_waitcnt vmcnt(6)
	v_mul_f32_e32 v140, v85, v85
	v_mul_f32_e32 v141, v87, v87
	v_fmac_f32_e32 v140, v84, v84
	v_fmac_f32_e32 v141, v86, v86
	v_add_f32_e32 v140, v140, v141
	v_add_f32_e32 v139, v139, v140
	s_waitcnt vmcnt(5)
	v_mul_f32_e32 v140, v89, v89
	v_mul_f32_e32 v141, v91, v91
	v_fmac_f32_e32 v140, v88, v88
	v_fmac_f32_e32 v141, v90, v90
	v_add_f32_e32 v140, v140, v141
	v_add_f32_e32 v138, v138, v140
	s_waitcnt vmcnt(4)
	v_mul_f32_e32 v140, v81, v81
	v_mul_f32_e32 v141, v83, v83
	v_fmac_f32_e32 v140, v80, v80
	v_fmac_f32_e32 v141, v82, v82
	v_add_f32_e32 v140, v140, v141
	v_add_f32_e32 v139, v139, v140
	s_waitcnt vmcnt(3)
	v_mul_f32_e32 v140, v77, v77
	v_mul_f32_e32 v141, v79, v79
	v_fmac_f32_e32 v140, v76, v76
	v_fmac_f32_e32 v141, v78, v78
	v_add_f32_e32 v140, v140, v141
	v_add_f32_e32 v138, v138, v140
	s_waitcnt vmcnt(2)
	v_mul_f32_e32 v140, v69, v69
	v_mul_f32_e32 v141, v71, v71
	v_fmac_f32_e32 v140, v68, v68
	v_fmac_f32_e32 v141, v70, v70
	v_add_f32_e32 v140, v140, v141
	v_add_f32_e32 v139, v139, v140
	s_waitcnt vmcnt(1)
	v_mul_f32_e32 v140, v73, v73
	v_mul_f32_e32 v141, v75, v75
	v_fmac_f32_e32 v140, v72, v72
	v_fmac_f32_e32 v141, v74, v74
	v_add_f32_e32 v140, v140, v141
	v_add_f32_e32 v138, v138, v140
	v_mov_b32_e32 v140, 0
	s_waitcnt vmcnt(0)
; #define LAS __attribute__((address_space(3)))
; template <int OUT, bool SRCBF>
; DI void nm_rowpair(LAS unsigned char* lds, const void* src0v, const void* src1v, bf16_t* b0, bf16_t* b1, unsigned char* q0, unsigned char* q1, int lane, float* sc0 = nullptr) {
;     ...
;     for (int j = 0; j < 8; ++j) { sa += (xa[j][0] * xa[j][0] + xa[j][1] * xa[j][1]) + (xa[j][2] * xa[j][2] + xa[j][3] * xa[j][3]); sb += (xb[j][0] * xb[j][0] + xb[j][1] * xb[j][1]) + (xb[j][2] * xb[j][2] + xb[j][3] * xb[j][3]); }
;     const float ra = 1.0f / sqrtf(wave_sum(sa) * (1.0f / D) + EPS), rb = 1.0f / sqrtf(wave_sum(sb) * (1.0f / D) + EPS);
;     if constexpr (OUT == 2) {
;         float ma = 0.f, mb = 0.f;
; #pragma unroll
;         for (int j = 0; j < 4; ++j) { const int c = 512 * j + 8 * lane;
;             const f32x4 A0 = *(const LAS f32x4*)(av + c), A1 = *(const LAS f32x4*)(av + c + 4), B0 = *(const LAS f32x4*)(bv + c), B1 = *(const LAS f32x4*)(bv + c + 4);
;             xa[2 * j] = xa[2 * j] * ra * A0 + B0; xa[2 * j + 1] = xa[2 * j + 1] * ra * A1 + B1; xb[2 * j] = xb[2 * j] * rb * A0 + B0; xb[2 * j + 1] = xb[2 * j + 1] * rb * A1 + B1;
; #pragma unroll
;             for (int e = 0; e < 4; ++e) { ma = fmaxf(ma, fmaxf(fabsf(xa[2 * j][e]), fabsf(xa[2 * j + 1][e]))); mb = fmaxf(mb, fmaxf(fabsf(xb[2 * j][e]), fabsf(xb[2 * j + 1][e]))); } }
	v_mul_f32_e32 v141, v65, v65
	v_add_f32_dpp v138, v138, v138 quad_perm:[1,0,3,2] row_mask:0xf bank_mask:0xf bound_ctrl:1
	v_mul_f32_e32 v142, v67, v67
	v_fmac_f32_e32 v141, v64, v64
	v_add_f32_dpp v138, v138, v138 quad_perm:[2,3,0,1] row_mask:0xf bank_mask:0xf bound_ctrl:1
	v_fmac_f32_e32 v142, v66, v66
	v_add_f32_e32 v141, v141, v142
	v_add_f32_dpp v138, v138, v138 row_ror:4 row_mask:0xf bank_mask:0xf bound_ctrl:1
	v_add_f32_e32 v139, v139, v141
	s_nop 0
	v_add_f32_dpp v138, v138, v138 row_ror:8 row_mask:0xf bank_mask:0xf bound_ctrl:1
	v_add_f32_dpp v139, v139, v139 quad_perm:[1,0,3,2] row_mask:0xf bank_mask:0xf bound_ctrl:1
	s_nop 0
	v_mov_b32_dpp v140, v138 row_bcast:15 row_mask:0xa bank_mask:0xf
	v_add_f32_e32 v138, v138, v140
	v_mov_b32_e32 v140, 0
	v_add_f32_dpp v139, v139, v139 quad_perm:[2,3,0,1] row_mask:0xf bank_mask:0xf bound_ctrl:1
	s_nop 0
	v_mov_b32_dpp v140, v138 row_bcast:31 row_mask:0xc bank_mask:0xf
	v_add_f32_e32 v138, v138, v140
	v_add_f32_dpp v139, v139, v139 row_ror:4 row_mask:0xf bank_mask:0xf bound_ctrl:1
	v_readlane_b32 s2, v138, 63
	s_nop 0
	v_add_f32_dpp v139, v139, v139 row_ror:8 row_mask:0xf bank_mask:0xf bound_ctrl:1
	v_fma_f32 v138, s2, v150, v129
	v_mul_f32_e32 v140, 0x4f800000, v138
	v_cmp_gt_f32_e32 vcc, s68, v138
	s_nop 1
	v_cndmask_b32_e32 v138, v138, v140, vcc
	v_sqrt_f32_e32 v140, v138
	s_nop 0
	v_add_u32_e32 v143, -1, v140
	v_fma_f32 v144, -v143, v140, v138
	v_cmp_ge_f32_e64 s[4:5], 0, v144
	v_add_u32_e32 v144, 1, v140
	s_nop 0
	v_cndmask_b32_e64 v143, v140, v143, s[4:5]
	v_fma_f32 v140, -v144, v140, v138
	v_cmp_lt_f32_e64 s[4:5], 0, v140
	s_nop 1
	v_cndmask_b32_e64 v140, v143, v144, s[4:5]
	v_mul_f32_e32 v143, 0x37800000, v140
	v_mov_b32_e32 v144, 0
	v_cndmask_b32_e32 v140, v140, v143, vcc
	v_cmp_class_f32_e32 vcc, v138, v148
	v_mov_b32_dpp v144, v139 row_bcast:15 row_mask:0xa bank_mask:0xf
	v_add_f32_e32 v139, v139, v144
	v_cndmask_b32_e32 v138, v140, v138, vcc
	v_mov_b32_e32 v144, 0
	v_div_scale_f32 v140, s[2:3], v138, v138, 1.0
	s_nop 0
	v_mov_b32_dpp v144, v139 row_bcast:31 row_mask:0xc bank_mask:0xf
	v_rcp_f32_e32 v143, v140
	v_add_f32_e32 v139, v139, v144
	v_fma_f32 v141, -v140, v143, 1.0
	v_readlane_b32 s2, v139, 63
	v_fmac_f32_e32 v143, v141, v143
	v_div_scale_f32 v141, vcc, 1.0, v138, 1.0
	v_fma_f32 v139, s2, v150, v129
	v_mul_f32_e32 v144, 0x4f800000, v139
	v_cmp_gt_f32_e64 s[4:5], s68, v139
	v_mul_f32_e32 v142, v141, v143
	v_fma_f32 v145, -v140, v142, v141
	v_cndmask_b32_e64 v139, v139, v144, s[4:5]
	v_sqrt_f32_e32 v144, v139
	v_fmac_f32_e32 v142, v145, v143
	v_fma_f32 v140, -v140, v142, v141
	v_div_fmas_f32 v140, v140, v143, v142
	v_add_u32_e32 v141, -1, v144
	v_fma_f32 v145, -v141, v144, v139
	v_cmp_ge_f32_e64 s[6:7], 0, v145
	v_add_u32_e32 v145, 1, v144
	v_div_fixup_f32 v154, v140, v138, 1.0
	v_cndmask_b32_e64 v141, v144, v141, s[6:7]
	v_fma_f32 v144, -v145, v144, v139
	v_cmp_lt_f32_e64 s[6:7], 0, v144
	v_pk_mul_f32 v[114:115], v[114:115], v[154:155] op_sel_hi:[1,0]
	v_pk_mul_f32 v[120:121], v[120:121], v[154:155] op_sel_hi:[1,0]
	v_cndmask_b32_e64 v141, v141, v145, s[6:7]
	v_mul_f32_e32 v144, 0x37800000, v141
	v_cndmask_b32_e64 v141, v141, v144, s[4:5]
	v_cmp_class_f32_e64 s[4:5], v139, v148
	v_pk_mul_f32 v[112:113], v[112:113], v[154:155] op_sel_hi:[1,0]
	v_pk_mul_f32 v[122:123], v[122:123], v[154:155] op_sel_hi:[1,0]
	v_cndmask_b32_e64 v139, v141, v139, s[4:5]
	v_div_scale_f32 v141, s[2:3], v139, v139, 1.0
	v_rcp_f32_e32 v144, v141
	s_nop 0
	v_fma_f32 v138, -v141, v144, 1.0
	v_fmac_f32_e32 v144, v138, v144
	v_div_scale_f32 v138, vcc, 1.0, v139, 1.0
	v_mul_f32_e32 v140, v138, v144
	v_fma_f32 v142, -v141, v140, v138
	v_fmac_f32_e32 v140, v142, v144
	v_fma_f32 v138, -v141, v140, v138
	v_div_fmas_f32 v138, v138, v144, v140
	v_div_fixup_f32 v156, v138, v139, 1.0
	s_waitcnt lgkmcnt(12)
	v_pk_fma_f32 v[138:139], v[114:115], v[6:7], v[14:15]
	v_pk_mul_f32 v[114:115], v[126:127], v[156:157] op_sel_hi:[1,0]
	v_pk_fma_f32 v[144:145], v[120:121], v[0:1], v[8:9]
	v_pk_fma_f32 v[140:141], v[112:113], v[4:5], v[12:13]
	v_pk_mul_f32 v[112:113], v[124:125], v[156:157] op_sel_hi:[1,0]
	v_pk_fma_f32 v[120:121], v[2:3], v[114:115], v[10:11]
	v_pk_mul_f32 v[114:115], v[116:117], v[156:157] op_sel_hi:[1,0]
	v_pk_fma_f32 v[142:143], v[122:123], v[2:3], v[10:11]
	v_pk_fma_f32 v[122:123], v[0:1], v[112:113], v[8:9]
	v_pk_mul_f32 v[112:113], v[118:119], v[156:157] op_sel_hi:[1,0]
	v_pk_fma_f32 v[114:115], v[4:5], v[114:115], v[12:13]
	v_max_f32_e64 v116, |v144|, |v140|
	v_max_f32_e64 v118, |v145|, |v141|
	v_max_f32_e64 v117, |v122|, |v114|
	v_max3_f32 v116, v116, 0, v118
	v_max_f32_e64 v118, |v123|, |v115|
	v_pk_fma_f32 v[112:113], v[6:7], v[112:113], v[14:15]
	v_max3_f32 v117, v117, 0, v118
	v_max_f32_e64 v118, |v142|, |v138|
	v_max_f32_e64 v124, |v143|, |v139|
	v_max_f32_e64 v119, |v120|, |v112|
	v_max3_f32 v118, v116, v118, v124
	v_max_f32_e64 v116, |v121|, |v113|
	v_max3_f32 v119, v117, v119, v116
	v_pk_mul_f32 v[116:117], v[108:109], v[154:155] op_sel_hi:[1,0]
	v_pk_mul_f32 v[108:109], v[110:111], v[154:155] op_sel_hi:[1,0]
	s_waitcnt lgkmcnt(9)
	v_pk_fma_f32 v[110:111], v[116:117], v[16:17], v[24:25]
	v_pk_mul_f32 v[116:117], v[104:105], v[154:155] op_sel_hi:[1,0]
	v_pk_mul_f32 v[104:105], v[106:107], v[154:155] op_sel_hi:[1,0]
	s_waitcnt lgkmcnt(8)
; #define LAS __attribute__((address_space(3)))
; template <int OUT, bool SRCBF>
; DI void nm_rowpair(LAS unsigned char* lds, const void* src0v, const void* src1v, bf16_t* b0, bf16_t* b1, unsigned char* q0, unsigned char* q1, int lane, float* sc0 = nullptr) {
;     ...
;         for (int j = 0; j < 4; ++j) { const int c = 512 * j + 8 * lane;
;             const f32x4 A0 = *(const LAS f32x4*)(av + c), A1 = *(const LAS f32x4*)(av + c + 4), B0 = *(const LAS f32x4*)(bv + c), B1 = *(const LAS f32x4*)(bv + c + 4);
;             xa[2 * j] = xa[2 * j] * ra * A0 + B0; xa[2 * j + 1] = xa[2 * j + 1] * ra * A1 + B1; xb[2 * j] = xb[2 * j] * rb * A0 + B0; xb[2 * j + 1] = xb[2 * j + 1] * rb * A1 + B1;
; #pragma unroll
;             for (int e = 0; e < 4; ++e) { ma = fmaxf(ma, fmaxf(fabsf(xa[2 * j][e]), fabsf(xa[2 * j + 1][e]))); mb = fmaxf(mb, fmaxf(fabsf(xb[2 * j][e]), fabsf(xb[2 * j + 1][e]))); } }
;         ma = wave_max(ma); mb = wave_max(mb);
;         const float ia = ma > 0.f ? 127.0f / ma : 0.f, ib = mb > 0.f ? 127.0f / mb : 0.f;
;         if (lane == 0) { sc0[0] = ma > 0.f ? ma * (1.0f / 127.0f) : 1.0f; sc0[1] = mb > 0.f ? mb * (1.0f / 127.0f) : 1.0f; }
	v_pk_fma_f32 v[106:107], v[116:117], v[20:21], v[28:29]
	v_pk_mul_f32 v[116:117], v[100:101], v[156:157] op_sel_hi:[1,0]
	v_pk_mul_f32 v[100:101], v[102:103], v[156:157] op_sel_hi:[1,0]
	v_pk_fma_f32 v[102:103], v[16:17], v[116:117], v[24:25]
	v_pk_mul_f32 v[116:117], v[96:97], v[156:157] op_sel_hi:[1,0]
	v_pk_mul_f32 v[96:97], v[98:99], v[156:157] op_sel_hi:[1,0]
	v_pk_fma_f32 v[98:99], v[20:21], v[116:117], v[28:29]
	v_max_f32_e64 v116, |v110|, |v106|
	v_max_f32_e64 v124, |v111|, |v107|
	v_pk_fma_f32 v[108:109], v[108:109], v[18:19], v[26:27]
	v_pk_fma_f32 v[104:105], v[104:105], v[22:23], v[30:31]
	v_max_f32_e64 v117, |v102|, |v98|
	v_max3_f32 v116, v118, v116, v124
	v_max_f32_e64 v118, |v103|, |v99|
	v_pk_fma_f32 v[100:101], v[18:19], v[100:101], v[26:27]
	v_pk_fma_f32 v[96:97], v[22:23], v[96:97], v[30:31]
	v_max3_f32 v117, v119, v117, v118
	v_max_f32_e64 v118, |v108|, |v104|
	v_max_f32_e64 v124, |v109|, |v105|
	v_max_f32_e64 v119, |v100|, |v96|
	v_max3_f32 v118, v116, v118, v124
	v_max_f32_e64 v116, |v101|, |v97|
	v_max3_f32 v119, v117, v119, v116
	v_pk_mul_f32 v[116:117], v[92:93], v[154:155] op_sel_hi:[1,0]
	v_pk_mul_f32 v[92:93], v[94:95], v[154:155] op_sel_hi:[1,0]
	s_waitcnt lgkmcnt(5)
	v_pk_fma_f32 v[94:95], v[116:117], v[32:33], v[40:41]
	v_pk_mul_f32 v[116:117], v[88:89], v[154:155] op_sel_hi:[1,0]
	v_pk_mul_f32 v[88:89], v[90:91], v[154:155] op_sel_hi:[1,0]
	s_waitcnt lgkmcnt(4)
	v_pk_fma_f32 v[90:91], v[116:117], v[36:37], v[44:45]
	v_pk_mul_f32 v[116:117], v[84:85], v[156:157] op_sel_hi:[1,0]
	v_pk_mul_f32 v[84:85], v[86:87], v[156:157] op_sel_hi:[1,0]
	v_pk_fma_f32 v[86:87], v[116:117], v[32:33], v[40:41]
	v_pk_mul_f32 v[116:117], v[80:81], v[156:157] op_sel_hi:[1,0]
	v_pk_mul_f32 v[80:81], v[82:83], v[156:157] op_sel_hi:[1,0]
	v_pk_fma_f32 v[82:83], v[116:117], v[36:37], v[44:45]
	v_max_f32_e64 v116, |v94|, |v90|
	v_max_f32_e64 v124, |v95|, |v91|
	v_pk_fma_f32 v[92:93], v[92:93], v[34:35], v[42:43]
	v_pk_fma_f32 v[88:89], v[88:89], v[38:39], v[46:47]
	v_max_f32_e64 v117, |v86|, |v82|
	v_max3_f32 v116, v118, v116, v124
	v_max_f32_e64 v118, |v87|, |v83|
	v_pk_fma_f32 v[84:85], v[84:85], v[34:35], v[42:43]
	v_pk_fma_f32 v[80:81], v[80:81], v[38:39], v[46:47]
	v_max3_f32 v117, v119, v117, v118
	v_max_f32_e64 v118, |v92|, |v88|
	v_max_f32_e64 v124, |v93|, |v89|
	v_max_f32_e64 v119, |v84|, |v80|
	v_max3_f32 v118, v116, v118, v124
	v_max_f32_e64 v116, |v85|, |v81|
	v_max3_f32 v119, v117, v119, v116
	v_pk_mul_f32 v[116:117], v[76:77], v[154:155] op_sel_hi:[1,0]
	v_pk_mul_f32 v[76:77], v[78:79], v[154:155] op_sel_hi:[1,0]
	s_waitcnt lgkmcnt(1)
	v_pk_fma_f32 v[78:79], v[116:117], v[48:49], v[56:57]
	v_pk_mul_f32 v[116:117], v[72:73], v[154:155] op_sel_hi:[1,0]
	v_pk_mul_f32 v[72:73], v[74:75], v[154:155] op_sel_hi:[1,0]
	s_waitcnt lgkmcnt(0)
	v_pk_fma_f32 v[74:75], v[116:117], v[52:53], v[60:61]
	v_pk_mul_f32 v[116:117], v[68:69], v[156:157] op_sel_hi:[1,0]
	v_pk_mul_f32 v[68:69], v[70:71], v[156:157] op_sel_hi:[1,0]
	v_pk_fma_f32 v[70:71], v[116:117], v[48:49], v[56:57]
	v_pk_mul_f32 v[116:117], v[64:65], v[156:157] op_sel_hi:[1,0]
	v_pk_mul_f32 v[64:65], v[66:67], v[156:157] op_sel_hi:[1,0]
	v_pk_fma_f32 v[66:67], v[116:117], v[52:53], v[60:61]
	v_max_f32_e64 v116, |v78|, |v74|
	v_max_f32_e64 v124, |v79|, |v75|
	v_pk_fma_f32 v[76:77], v[76:77], v[50:51], v[58:59]
	v_pk_fma_f32 v[72:73], v[72:73], v[54:55], v[62:63]
	v_max_f32_e64 v117, |v70|, |v66|
	v_max3_f32 v116, v118, v116, v124
	v_max_f32_e64 v118, |v71|, |v67|
	v_pk_fma_f32 v[68:69], v[68:69], v[50:51], v[58:59]
	v_pk_fma_f32 v[64:65], v[64:65], v[54:55], v[62:63]
	v_max3_f32 v117, v119, v117, v118
	v_max_f32_e64 v118, |v76|, |v72|
	v_max_f32_e64 v124, |v77|, |v73|
	v_max_f32_e64 v119, |v68|, |v64|
	v_max3_f32 v116, v116, v118, v124
	v_max_f32_e64 v118, |v69|, |v65|
	v_max3_f32 v117, v117, v119, v118
	v_mov_b32_e32 v118, 0
	s_nop 1
	v_mov_b32_dpp v118, v116 quad_perm:[1,0,3,2] row_mask:0xf bank_mask:0xf
	v_max_f32_e32 v118, v118, v118
	v_max_f32_e32 v116, v116, v118
	v_mov_b32_e32 v118, 0
	s_nop 1
	v_mov_b32_dpp v118, v116 quad_perm:[2,3,0,1] row_mask:0xf bank_mask:0xf
	v_max_f32_e32 v118, v118, v118
	v_max_f32_e32 v116, v116, v118
	v_mov_b32_e32 v118, 0
	s_nop 1
	v_mov_b32_dpp v118, v116 row_ror:4 row_mask:0xf bank_mask:0xf
	v_max_f32_e32 v118, v118, v118
	v_max_f32_e32 v116, v116, v118
	v_mov_b32_e32 v118, 0
	s_nop 1
	v_mov_b32_dpp v118, v116 row_ror:8 row_mask:0xf bank_mask:0xf
	v_max_f32_e32 v118, v118, v118
	v_max_f32_e32 v116, v116, v118
	v_mov_b32_e32 v118, 0
	s_nop 1
	v_mov_b32_dpp v118, v116 row_bcast:15 row_mask:0xa bank_mask:0xf
	v_max_f32_e32 v118, v118, v118
	v_max_f32_e32 v116, v116, v118
	v_mov_b32_e32 v118, 0
	s_nop 1
	v_mov_b32_dpp v118, v116 row_bcast:31 row_mask:0xc bank_mask:0xf
	v_max_f32_e32 v118, v118, v118
	v_max_f32_e32 v116, v116, v118
	s_nop 0
	v_readlane_b32 s12, v116, 63
	v_mov_b32_e32 v116, 0
	s_nop 0
	v_cmp_gt_f32_e64 s[4:5], s12, 0
	v_mov_b32_dpp v116, v117 quad_perm:[1,0,3,2] row_mask:0xf bank_mask:0xf
	v_max_f32_e32 v116, v116, v116
	v_max_f32_e32 v116, v117, v116
	v_mov_b32_e32 v117, 0
	s_nop 1
	v_mov_b32_dpp v117, v116 quad_perm:[2,3,0,1] row_mask:0xf bank_mask:0xf
	v_max_f32_e32 v117, v117, v117
	v_max_f32_e32 v116, v116, v117
	v_mov_b32_e32 v117, 0
	s_nop 1
	v_mov_b32_dpp v117, v116 row_ror:4 row_mask:0xf bank_mask:0xf
	v_max_f32_e32 v117, v117, v117
	v_max_f32_e32 v116, v116, v117
	v_mov_b32_e32 v117, 0
	s_nop 1
	v_mov_b32_dpp v117, v116 row_ror:8 row_mask:0xf bank_mask:0xf
	v_max_f32_e32 v117, v117, v117
	v_max_f32_e32 v116, v116, v117
	v_mov_b32_e32 v117, 0
	s_nop 1
	v_mov_b32_dpp v117, v116 row_bcast:15 row_mask:0xa bank_mask:0xf
	v_max_f32_e32 v117, v117, v117
	v_max_f32_e32 v116, v116, v117
	v_mov_b32_e32 v117, 0
	s_nop 1
	v_mov_b32_dpp v117, v116 row_bcast:31 row_mask:0xc bank_mask:0xf
	v_max_f32_e32 v117, v117, v117
	v_max_f32_e32 v116, v116, v117
	s_nop 0
	v_readlane_b32 s15, v116, 63
	s_nop 1
	v_cmp_gt_f32_e64 s[6:7], s15, 0
	s_and_saveexec_b64 s[2:3], s[0:1]
	s_cbranch_execz .LBB0_205
	v_readlane_b32 s76, v254, 2
	v_readlane_b32 s78, v254, 4
	v_mul_f32_e32 v116, s15, v151
	v_readlane_b32 s79, v254, 5
	s_add_u32 s74, s78, s56
	v_cndmask_b32_e64 v117, 1.0, v116, s[6:7]
	v_mul_f32_e32 v116, s12, v151
	s_addc_u32 s75, s79, s57
	v_cndmask_b32_e64 v116, 1.0, v116, s[4:5]
	v_readlane_b32 s77, v254, 3
	global_store_dwordx2 v149, v[116:117], s[74:75]
	s_branch .LBB0_205
